# speedup vs baseline: 1.0202x; 1.0202x over previous
_Z7k1_projPKfPKDv8_DF16_S0_S0_S0_PS1_S4_S4_:
	s_load_dwordx8 s[12:19], s[0:1], 0x0
	s_load_dwordx8 s[4:11], s[0:1], 0x20
	v_mov_b32_e32 v182, v0
	v_and_b32_e32 v181, 63, v0
	v_lshrrev_b32_e32 v183, 6, v0
	v_lshlrev_b32_e32 v180, 4, v181
	s_lshr_b32 s20, s2, 6
	s_and_b32 s21, s2, 63
	v_readfirstlane_b32 s22, v183
	s_nop 3
	s_waitcnt lgkmcnt(0)
	s_cmp_lt_u32 s22, 4
	s_cbranch_scc0 .Lk1_loader
	s_lshl_b32 s23, s22, 15
	s_add_u32 s24, s14, s23
	s_addc_u32 s25, s15, 0
	s_add_u32 s26, s24, 0x20000
	s_addc_u32 s27, s25, 0
	s_add_u32 s28, s24, 0x40000
	s_addc_u32 s29, s25, 0
	s_cmp_lt_u32 s22, 2
	s_cselect_b32 s30, s16, s18
	s_cselect_b32 s31, s17, s19
	s_and_b32 s23, s22, 1
	s_lshl_b32 s23, s23, 7
	s_add_u32 s30, s30, s23
	s_addc_u32 s31, s31, 0
	v_lshrrev_b32_e32 v184, 5, v181
	v_lshlrev_b32_e32 v184, 4, v184
	global_load_dwordx4 v[0:3], v184, s[30:31] offset:0
	global_load_dwordx4 v[4:7], v184, s[30:31] offset:32
	global_load_dwordx4 v[8:11], v184, s[30:31] offset:64
	global_load_dwordx4 v[12:15], v184, s[30:31] offset:96
	v_and_b32_e32 v185, 31, v181
	v_lshlrev_b32_e32 v185, 2, v185
	s_lshl_b32 s23, s22, 7
	s_add_u32 s32, s4, s23
	s_addc_u32 s33, s5, 0
	global_load_dword v32, v185, s[32:33]
	global_load_dword v64, v185, s[32:33] offset:512
	global_load_dwordx4 v[96:99], v180, s[24:25] offset:0
	global_load_dwordx4 v[100:103], v180, s[26:27] offset:0
	global_load_dwordx4 v[104:107], v180, s[28:29] offset:0
	global_load_dwordx4 v[108:111], v180, s[24:25] offset:1024
	global_load_dwordx4 v[112:115], v180, s[26:27] offset:1024
	global_load_dwordx4 v[116:119], v180, s[28:29] offset:1024
	global_load_dwordx4 v[120:123], v180, s[24:25] offset:2048
	global_load_dwordx4 v[124:127], v180, s[26:27] offset:2048
	global_load_dwordx4 v[128:131], v180, s[28:29] offset:2048
	global_load_dwordx4 v[132:135], v180, s[24:25] offset:3072
	global_load_dwordx4 v[136:139], v180, s[26:27] offset:3072
	global_load_dwordx4 v[140:143], v180, s[28:29] offset:3072
	s_add_u32 s24, s24, 0x1000
	s_addc_u32 s25, s25, 0
	s_add_u32 s26, s26, 0x1000
	s_addc_u32 s27, s27, 0
	s_add_u32 s28, s28, 0x1000
	s_addc_u32 s29, s29, 0
	s_waitcnt vmcnt(12)
	v_mov_b32_e32 v16, v0
	v_mov_b32_e32 v17, v1
	v_mov_b32_e32 v18, v2
	v_mov_b32_e32 v19, v3
	v_mov_b32_e32 v20, v4
	v_mov_b32_e32 v21, v5
	v_mov_b32_e32 v22, v6
	v_mov_b32_e32 v23, v7
	v_mov_b32_e32 v24, v8
	v_mov_b32_e32 v25, v9
	v_mov_b32_e32 v26, v10
	v_mov_b32_e32 v27, v11
	v_mov_b32_e32 v28, v12
	v_mov_b32_e32 v29, v13
	v_mov_b32_e32 v30, v14
	v_mov_b32_e32 v31, v15
	v_mov_b32_e32 v33, v32
	v_mov_b32_e32 v34, v32
	v_mov_b32_e32 v35, v32
	v_mov_b32_e32 v36, v32
	v_mov_b32_e32 v37, v32
	v_mov_b32_e32 v38, v32
	v_mov_b32_e32 v39, v32
	v_mov_b32_e32 v40, v32
	v_mov_b32_e32 v41, v32
	v_mov_b32_e32 v42, v32
	v_mov_b32_e32 v43, v32
	v_mov_b32_e32 v44, v32
	v_mov_b32_e32 v45, v32
	v_mov_b32_e32 v46, v32
	v_mov_b32_e32 v47, v32
	v_mov_b32_e32 v48, v32
	v_mov_b32_e32 v49, v32
	v_mov_b32_e32 v50, v32
	v_mov_b32_e32 v51, v32
	v_mov_b32_e32 v52, v32
	v_mov_b32_e32 v53, v32
	v_mov_b32_e32 v54, v32
	v_mov_b32_e32 v55, v32
	v_mov_b32_e32 v56, v32
	v_mov_b32_e32 v57, v32
	v_mov_b32_e32 v58, v32
	v_mov_b32_e32 v59, v32
	v_mov_b32_e32 v60, v32
	v_mov_b32_e32 v61, v32
	v_mov_b32_e32 v62, v32
	v_mov_b32_e32 v63, v32
	v_mov_b32_e32 v65, v64
	v_mov_b32_e32 v66, v64
	v_mov_b32_e32 v67, v64
	v_mov_b32_e32 v68, v64
	v_mov_b32_e32 v69, v64
	v_mov_b32_e32 v70, v64
	v_mov_b32_e32 v71, v64
	v_mov_b32_e32 v72, v64
	v_mov_b32_e32 v73, v64
	v_mov_b32_e32 v74, v64
	v_mov_b32_e32 v75, v64
	v_mov_b32_e32 v76, v64
	v_mov_b32_e32 v77, v64
	v_mov_b32_e32 v78, v64
	v_mov_b32_e32 v79, v64
	v_mov_b32_e32 v80, v64
	v_mov_b32_e32 v81, v64
	v_mov_b32_e32 v82, v64
	v_mov_b32_e32 v83, v64
	v_mov_b32_e32 v84, v64
	v_mov_b32_e32 v85, v64
	v_mov_b32_e32 v86, v64
	v_mov_b32_e32 v87, v64
	v_mov_b32_e32 v88, v64
	v_mov_b32_e32 v89, v64
	v_mov_b32_e32 v90, v64
	v_mov_b32_e32 v91, v64
	v_mov_b32_e32 v92, v64
	v_mov_b32_e32 v93, v64
	v_mov_b32_e32 v94, v64
	v_mov_b32_e32 v95, v64
	s_barrier
	ds_read_b128 v[156:159], v180 offset:0
	ds_read_b128 v[160:163], v180 offset:32768
	ds_read_b128 v[164:167], v180 offset:1024
	ds_read_b128 v[168:171], v180 offset:33792
	global_load_dwordx4 v[144:147], v180, s[24:25] offset:0
	global_load_dwordx4 v[148:151], v180, s[26:27] offset:0
	global_load_dwordx4 v[152:155], v180, s[28:29] offset:0
	ds_read_b128 v[172:175], v180 offset:2048
	ds_read_b128 v[176:179], v180 offset:34816
	s_waitcnt vmcnt(12)
	s_waitcnt lgkmcnt(4)
	v_mfma_f32_32x32x16_f16 v[0:15], v[96:99], v[156:159], v[0:15]
	v_mfma_f32_32x32x16_f16 v[32:47], v[156:159], v[100:103], v[32:47]
	v_mfma_f32_32x32x16_f16 v[64:79], v[156:159], v[104:107], v[64:79]
	v_mfma_f32_32x32x16_f16 v[16:31], v[96:99], v[160:163], v[16:31]
	v_mfma_f32_32x32x16_f16 v[48:63], v[160:163], v[100:103], v[48:63]
	v_mfma_f32_32x32x16_f16 v[80:95], v[160:163], v[104:107], v[80:95]
	global_load_dwordx4 v[96:99], v180, s[24:25] offset:1024
	global_load_dwordx4 v[100:103], v180, s[26:27] offset:1024
	global_load_dwordx4 v[104:107], v180, s[28:29] offset:1024
	ds_read_b128 v[156:159], v180 offset:3072
	ds_read_b128 v[160:163], v180 offset:35840
	s_waitcnt vmcnt(12)
	s_waitcnt lgkmcnt(4)
	v_mfma_f32_32x32x16_f16 v[0:15], v[108:111], v[164:167], v[0:15]
	v_mfma_f32_32x32x16_f16 v[32:47], v[164:167], v[112:115], v[32:47]
	v_mfma_f32_32x32x16_f16 v[64:79], v[164:167], v[116:119], v[64:79]
	v_mfma_f32_32x32x16_f16 v[16:31], v[108:111], v[168:171], v[16:31]
	v_mfma_f32_32x32x16_f16 v[48:63], v[168:171], v[112:115], v[48:63]
	v_mfma_f32_32x32x16_f16 v[80:95], v[168:171], v[116:119], v[80:95]
	global_load_dwordx4 v[108:111], v180, s[24:25] offset:2048
	global_load_dwordx4 v[112:115], v180, s[26:27] offset:2048
	global_load_dwordx4 v[116:119], v180, s[28:29] offset:2048
	ds_read_b128 v[164:167], v180 offset:4096
	ds_read_b128 v[168:171], v180 offset:36864
	s_waitcnt vmcnt(12)
	s_waitcnt lgkmcnt(4)
	v_mfma_f32_32x32x16_f16 v[0:15], v[120:123], v[172:175], v[0:15]
	v_mfma_f32_32x32x16_f16 v[32:47], v[172:175], v[124:127], v[32:47]
	v_mfma_f32_32x32x16_f16 v[64:79], v[172:175], v[128:131], v[64:79]
	v_mfma_f32_32x32x16_f16 v[16:31], v[120:123], v[176:179], v[16:31]
	v_mfma_f32_32x32x16_f16 v[48:63], v[176:179], v[124:127], v[48:63]
	v_mfma_f32_32x32x16_f16 v[80:95], v[176:179], v[128:131], v[80:95]
	global_load_dwordx4 v[120:123], v180, s[24:25] offset:3072
	global_load_dwordx4 v[124:127], v180, s[26:27] offset:3072
	global_load_dwordx4 v[128:131], v180, s[28:29] offset:3072
	s_add_u32 s24, s24, 0x1000
	s_addc_u32 s25, s25, 0
	s_add_u32 s26, s26, 0x1000
	s_addc_u32 s27, s27, 0
	s_add_u32 s28, s28, 0x1000
	s_addc_u32 s29, s29, 0
	ds_read_b128 v[172:175], v180 offset:5120
	ds_read_b128 v[176:179], v180 offset:37888
	s_waitcnt vmcnt(12)
	s_waitcnt lgkmcnt(4)
	v_mfma_f32_32x32x16_f16 v[0:15], v[132:135], v[156:159], v[0:15]
	v_mfma_f32_32x32x16_f16 v[32:47], v[156:159], v[136:139], v[32:47]
	v_mfma_f32_32x32x16_f16 v[64:79], v[156:159], v[140:143], v[64:79]
	v_mfma_f32_32x32x16_f16 v[16:31], v[132:135], v[160:163], v[16:31]
	v_mfma_f32_32x32x16_f16 v[48:63], v[160:163], v[136:139], v[48:63]
	v_mfma_f32_32x32x16_f16 v[80:95], v[160:163], v[140:143], v[80:95]
	global_load_dwordx4 v[132:135], v180, s[24:25] offset:0
	global_load_dwordx4 v[136:139], v180, s[26:27] offset:0
	global_load_dwordx4 v[140:143], v180, s[28:29] offset:0
	ds_read_b128 v[156:159], v180 offset:6144
	ds_read_b128 v[160:163], v180 offset:38912
	s_waitcnt vmcnt(12)
	s_waitcnt lgkmcnt(4)
	v_mfma_f32_32x32x16_f16 v[0:15], v[144:147], v[164:167], v[0:15]
	v_mfma_f32_32x32x16_f16 v[32:47], v[164:167], v[148:151], v[32:47]
	v_mfma_f32_32x32x16_f16 v[64:79], v[164:167], v[152:155], v[64:79]
	v_mfma_f32_32x32x16_f16 v[16:31], v[144:147], v[168:171], v[16:31]
	v_mfma_f32_32x32x16_f16 v[48:63], v[168:171], v[148:151], v[48:63]
	v_mfma_f32_32x32x16_f16 v[80:95], v[168:171], v[152:155], v[80:95]
	global_load_dwordx4 v[144:147], v180, s[24:25] offset:1024
	global_load_dwordx4 v[148:151], v180, s[26:27] offset:1024
	global_load_dwordx4 v[152:155], v180, s[28:29] offset:1024
	ds_read_b128 v[164:167], v180 offset:7168
	ds_read_b128 v[168:171], v180 offset:39936
	s_waitcnt vmcnt(12)
	s_waitcnt lgkmcnt(4)
	v_mfma_f32_32x32x16_f16 v[0:15], v[96:99], v[172:175], v[0:15]
	v_mfma_f32_32x32x16_f16 v[32:47], v[172:175], v[100:103], v[32:47]
	v_mfma_f32_32x32x16_f16 v[64:79], v[172:175], v[104:107], v[64:79]
	v_mfma_f32_32x32x16_f16 v[16:31], v[96:99], v[176:179], v[16:31]
	v_mfma_f32_32x32x16_f16 v[48:63], v[176:179], v[100:103], v[48:63]
	v_mfma_f32_32x32x16_f16 v[80:95], v[176:179], v[104:107], v[80:95]
	global_load_dwordx4 v[96:99], v180, s[24:25] offset:2048
	global_load_dwordx4 v[100:103], v180, s[26:27] offset:2048
	global_load_dwordx4 v[104:107], v180, s[28:29] offset:2048
	s_waitcnt vmcnt(12)
	s_waitcnt lgkmcnt(2)
	v_mfma_f32_32x32x16_f16 v[0:15], v[108:111], v[156:159], v[0:15]
	v_mfma_f32_32x32x16_f16 v[32:47], v[156:159], v[112:115], v[32:47]
	v_mfma_f32_32x32x16_f16 v[64:79], v[156:159], v[116:119], v[64:79]
	v_mfma_f32_32x32x16_f16 v[16:31], v[108:111], v[160:163], v[16:31]
	v_mfma_f32_32x32x16_f16 v[48:63], v[160:163], v[112:115], v[48:63]
	v_mfma_f32_32x32x16_f16 v[80:95], v[160:163], v[116:119], v[80:95]
	global_load_dwordx4 v[108:111], v180, s[24:25] offset:3072
	global_load_dwordx4 v[112:115], v180, s[26:27] offset:3072
	global_load_dwordx4 v[116:119], v180, s[28:29] offset:3072
	s_add_u32 s24, s24, 0x1000
	s_addc_u32 s25, s25, 0
	s_add_u32 s26, s26, 0x1000
	s_addc_u32 s27, s27, 0
	s_add_u32 s28, s28, 0x1000
	s_addc_u32 s29, s29, 0
	s_waitcnt vmcnt(12)
	s_waitcnt lgkmcnt(0)
	v_mfma_f32_32x32x16_f16 v[0:15], v[120:123], v[164:167], v[0:15]
	v_mfma_f32_32x32x16_f16 v[32:47], v[164:167], v[124:127], v[32:47]
	v_mfma_f32_32x32x16_f16 v[64:79], v[164:167], v[128:131], v[64:79]
	v_mfma_f32_32x32x16_f16 v[16:31], v[120:123], v[168:171], v[16:31]
	v_mfma_f32_32x32x16_f16 v[48:63], v[168:171], v[124:127], v[48:63]
	v_mfma_f32_32x32x16_f16 v[80:95], v[168:171], v[128:131], v[80:95]
	s_barrier
	ds_read_b128 v[172:175], v180 offset:8192
	ds_read_b128 v[176:179], v180 offset:40960
	ds_read_b128 v[156:159], v180 offset:9216
	ds_read_b128 v[160:163], v180 offset:41984
	global_load_dwordx4 v[120:123], v180, s[24:25] offset:0
	global_load_dwordx4 v[124:127], v180, s[26:27] offset:0
	global_load_dwordx4 v[128:131], v180, s[28:29] offset:0
	ds_read_b128 v[164:167], v180 offset:10240
	ds_read_b128 v[168:171], v180 offset:43008
	s_waitcnt vmcnt(12)
	s_waitcnt lgkmcnt(4)
	v_mfma_f32_32x32x16_f16 v[0:15], v[132:135], v[172:175], v[0:15]
	v_mfma_f32_32x32x16_f16 v[32:47], v[172:175], v[136:139], v[32:47]
	v_mfma_f32_32x32x16_f16 v[64:79], v[172:175], v[140:143], v[64:79]
	v_mfma_f32_32x32x16_f16 v[16:31], v[132:135], v[176:179], v[16:31]
	v_mfma_f32_32x32x16_f16 v[48:63], v[176:179], v[136:139], v[48:63]
	v_mfma_f32_32x32x16_f16 v[80:95], v[176:179], v[140:143], v[80:95]
	global_load_dwordx4 v[132:135], v180, s[24:25] offset:1024
	global_load_dwordx4 v[136:139], v180, s[26:27] offset:1024
	global_load_dwordx4 v[140:143], v180, s[28:29] offset:1024
	ds_read_b128 v[172:175], v180 offset:11264
	ds_read_b128 v[176:179], v180 offset:44032
	s_waitcnt vmcnt(12)
	s_waitcnt lgkmcnt(4)
	v_mfma_f32_32x32x16_f16 v[0:15], v[144:147], v[156:159], v[0:15]
	v_mfma_f32_32x32x16_f16 v[32:47], v[156:159], v[148:151], v[32:47]
	v_mfma_f32_32x32x16_f16 v[64:79], v[156:159], v[152:155], v[64:79]
	v_mfma_f32_32x32x16_f16 v[16:31], v[144:147], v[160:163], v[16:31]
	v_mfma_f32_32x32x16_f16 v[48:63], v[160:163], v[148:151], v[48:63]
	v_mfma_f32_32x32x16_f16 v[80:95], v[160:163], v[152:155], v[80:95]
	global_load_dwordx4 v[144:147], v180, s[24:25] offset:2048
	global_load_dwordx4 v[148:151], v180, s[26:27] offset:2048
	global_load_dwordx4 v[152:155], v180, s[28:29] offset:2048
	ds_read_b128 v[156:159], v180 offset:12288
	ds_read_b128 v[160:163], v180 offset:45056
	s_waitcnt vmcnt(12)
	s_waitcnt lgkmcnt(4)
	v_mfma_f32_32x32x16_f16 v[0:15], v[96:99], v[164:167], v[0:15]
	v_mfma_f32_32x32x16_f16 v[32:47], v[164:167], v[100:103], v[32:47]
	v_mfma_f32_32x32x16_f16 v[64:79], v[164:167], v[104:107], v[64:79]
	v_mfma_f32_32x32x16_f16 v[16:31], v[96:99], v[168:171], v[16:31]
	v_mfma_f32_32x32x16_f16 v[48:63], v[168:171], v[100:103], v[48:63]
	v_mfma_f32_32x32x16_f16 v[80:95], v[168:171], v[104:107], v[80:95]
	global_load_dwordx4 v[96:99], v180, s[24:25] offset:3072
	global_load_dwordx4 v[100:103], v180, s[26:27] offset:3072
	global_load_dwordx4 v[104:107], v180, s[28:29] offset:3072
	s_add_u32 s24, s24, 0x1000
	s_addc_u32 s25, s25, 0
	s_add_u32 s26, s26, 0x1000
	s_addc_u32 s27, s27, 0
	s_add_u32 s28, s28, 0x1000
	s_addc_u32 s29, s29, 0
	ds_read_b128 v[164:167], v180 offset:13312
	ds_read_b128 v[168:171], v180 offset:46080
	s_waitcnt vmcnt(12)
	s_waitcnt lgkmcnt(4)
	v_mfma_f32_32x32x16_f16 v[0:15], v[108:111], v[172:175], v[0:15]
	v_mfma_f32_32x32x16_f16 v[32:47], v[172:175], v[112:115], v[32:47]
	v_mfma_f32_32x32x16_f16 v[64:79], v[172:175], v[116:119], v[64:79]
	v_mfma_f32_32x32x16_f16 v[16:31], v[108:111], v[176:179], v[16:31]
	v_mfma_f32_32x32x16_f16 v[48:63], v[176:179], v[112:115], v[48:63]
	v_mfma_f32_32x32x16_f16 v[80:95], v[176:179], v[116:119], v[80:95]
	global_load_dwordx4 v[108:111], v180, s[24:25] offset:0
	global_load_dwordx4 v[112:115], v180, s[26:27] offset:0
	global_load_dwordx4 v[116:119], v180, s[28:29] offset:0
	ds_read_b128 v[172:175], v180 offset:14336
	ds_read_b128 v[176:179], v180 offset:47104
	s_waitcnt vmcnt(12)
	s_waitcnt lgkmcnt(4)
	v_mfma_f32_32x32x16_f16 v[0:15], v[120:123], v[156:159], v[0:15]
	v_mfma_f32_32x32x16_f16 v[32:47], v[156:159], v[124:127], v[32:47]
	v_mfma_f32_32x32x16_f16 v[64:79], v[156:159], v[128:131], v[64:79]
	v_mfma_f32_32x32x16_f16 v[16:31], v[120:123], v[160:163], v[16:31]
	v_mfma_f32_32x32x16_f16 v[48:63], v[160:163], v[124:127], v[48:63]
	v_mfma_f32_32x32x16_f16 v[80:95], v[160:163], v[128:131], v[80:95]
	global_load_dwordx4 v[120:123], v180, s[24:25] offset:1024
	global_load_dwordx4 v[124:127], v180, s[26:27] offset:1024
	global_load_dwordx4 v[128:131], v180, s[28:29] offset:1024
	ds_read_b128 v[156:159], v180 offset:15360
	ds_read_b128 v[160:163], v180 offset:48128
	s_waitcnt vmcnt(12)
	s_waitcnt lgkmcnt(4)
	v_mfma_f32_32x32x16_f16 v[0:15], v[132:135], v[164:167], v[0:15]
	v_mfma_f32_32x32x16_f16 v[32:47], v[164:167], v[136:139], v[32:47]
	v_mfma_f32_32x32x16_f16 v[64:79], v[164:167], v[140:143], v[64:79]
	v_mfma_f32_32x32x16_f16 v[16:31], v[132:135], v[168:171], v[16:31]
	v_mfma_f32_32x32x16_f16 v[48:63], v[168:171], v[136:139], v[48:63]
	v_mfma_f32_32x32x16_f16 v[80:95], v[168:171], v[140:143], v[80:95]
	global_load_dwordx4 v[132:135], v180, s[24:25] offset:2048
	global_load_dwordx4 v[136:139], v180, s[26:27] offset:2048
	global_load_dwordx4 v[140:143], v180, s[28:29] offset:2048
	s_waitcnt vmcnt(12)
	s_waitcnt lgkmcnt(2)
	v_mfma_f32_32x32x16_f16 v[0:15], v[144:147], v[172:175], v[0:15]
	v_mfma_f32_32x32x16_f16 v[32:47], v[172:175], v[148:151], v[32:47]
	v_mfma_f32_32x32x16_f16 v[64:79], v[172:175], v[152:155], v[64:79]
	v_mfma_f32_32x32x16_f16 v[16:31], v[144:147], v[176:179], v[16:31]
	v_mfma_f32_32x32x16_f16 v[48:63], v[176:179], v[148:151], v[48:63]
	v_mfma_f32_32x32x16_f16 v[80:95], v[176:179], v[152:155], v[80:95]
	global_load_dwordx4 v[144:147], v180, s[24:25] offset:3072
	global_load_dwordx4 v[148:151], v180, s[26:27] offset:3072
	global_load_dwordx4 v[152:155], v180, s[28:29] offset:3072
	s_add_u32 s24, s24, 0x1000
	s_addc_u32 s25, s25, 0
	s_add_u32 s26, s26, 0x1000
	s_addc_u32 s27, s27, 0
	s_add_u32 s28, s28, 0x1000
	s_addc_u32 s29, s29, 0
	s_waitcnt vmcnt(12)
	s_waitcnt lgkmcnt(0)
	v_mfma_f32_32x32x16_f16 v[0:15], v[96:99], v[156:159], v[0:15]
	v_mfma_f32_32x32x16_f16 v[32:47], v[156:159], v[100:103], v[32:47]
	v_mfma_f32_32x32x16_f16 v[64:79], v[156:159], v[104:107], v[64:79]
	v_mfma_f32_32x32x16_f16 v[16:31], v[96:99], v[160:163], v[16:31]
	v_mfma_f32_32x32x16_f16 v[48:63], v[160:163], v[100:103], v[48:63]
	v_mfma_f32_32x32x16_f16 v[80:95], v[160:163], v[104:107], v[80:95]
	s_barrier
	ds_read_b128 v[164:167], v180 offset:16384
	ds_read_b128 v[168:171], v180 offset:49152
	ds_read_b128 v[172:175], v180 offset:17408
	ds_read_b128 v[176:179], v180 offset:50176
	global_load_dwordx4 v[96:99], v180, s[24:25] offset:0
	global_load_dwordx4 v[100:103], v180, s[26:27] offset:0
	global_load_dwordx4 v[104:107], v180, s[28:29] offset:0
	ds_read_b128 v[156:159], v180 offset:18432
	ds_read_b128 v[160:163], v180 offset:51200
	s_waitcnt vmcnt(12)
	s_waitcnt lgkmcnt(4)
	v_mfma_f32_32x32x16_f16 v[0:15], v[108:111], v[164:167], v[0:15]
	v_mfma_f32_32x32x16_f16 v[32:47], v[164:167], v[112:115], v[32:47]
	v_mfma_f32_32x32x16_f16 v[64:79], v[164:167], v[116:119], v[64:79]
	v_mfma_f32_32x32x16_f16 v[16:31], v[108:111], v[168:171], v[16:31]
	v_mfma_f32_32x32x16_f16 v[48:63], v[168:171], v[112:115], v[48:63]
	v_mfma_f32_32x32x16_f16 v[80:95], v[168:171], v[116:119], v[80:95]
	global_load_dwordx4 v[108:111], v180, s[24:25] offset:1024
	global_load_dwordx4 v[112:115], v180, s[26:27] offset:1024
	global_load_dwordx4 v[116:119], v180, s[28:29] offset:1024
	ds_read_b128 v[164:167], v180 offset:19456
	ds_read_b128 v[168:171], v180 offset:52224
	s_waitcnt vmcnt(12)
	s_waitcnt lgkmcnt(4)
	v_mfma_f32_32x32x16_f16 v[0:15], v[120:123], v[172:175], v[0:15]
	v_mfma_f32_32x32x16_f16 v[32:47], v[172:175], v[124:127], v[32:47]
	v_mfma_f32_32x32x16_f16 v[64:79], v[172:175], v[128:131], v[64:79]
	v_mfma_f32_32x32x16_f16 v[16:31], v[120:123], v[176:179], v[16:31]
	v_mfma_f32_32x32x16_f16 v[48:63], v[176:179], v[124:127], v[48:63]
	v_mfma_f32_32x32x16_f16 v[80:95], v[176:179], v[128:131], v[80:95]
	global_load_dwordx4 v[120:123], v180, s[24:25] offset:2048
	global_load_dwordx4 v[124:127], v180, s[26:27] offset:2048
	global_load_dwordx4 v[128:131], v180, s[28:29] offset:2048
	ds_read_b128 v[172:175], v180 offset:20480
	ds_read_b128 v[176:179], v180 offset:53248
	s_waitcnt vmcnt(12)
	s_waitcnt lgkmcnt(4)
	v_mfma_f32_32x32x16_f16 v[0:15], v[132:135], v[156:159], v[0:15]
	v_mfma_f32_32x32x16_f16 v[32:47], v[156:159], v[136:139], v[32:47]
	v_mfma_f32_32x32x16_f16 v[64:79], v[156:159], v[140:143], v[64:79]
	v_mfma_f32_32x32x16_f16 v[16:31], v[132:135], v[160:163], v[16:31]
	v_mfma_f32_32x32x16_f16 v[48:63], v[160:163], v[136:139], v[48:63]
	v_mfma_f32_32x32x16_f16 v[80:95], v[160:163], v[140:143], v[80:95]
	global_load_dwordx4 v[132:135], v180, s[24:25] offset:3072
	global_load_dwordx4 v[136:139], v180, s[26:27] offset:3072
	global_load_dwordx4 v[140:143], v180, s[28:29] offset:3072
	s_add_u32 s24, s24, 0x1000
	s_addc_u32 s25, s25, 0
	s_add_u32 s26, s26, 0x1000
	s_addc_u32 s27, s27, 0
	s_add_u32 s28, s28, 0x1000
	s_addc_u32 s29, s29, 0
	ds_read_b128 v[156:159], v180 offset:21504
	ds_read_b128 v[160:163], v180 offset:54272
	s_waitcnt vmcnt(12)
	s_waitcnt lgkmcnt(4)
	v_mfma_f32_32x32x16_f16 v[0:15], v[144:147], v[164:167], v[0:15]
	v_mfma_f32_32x32x16_f16 v[32:47], v[164:167], v[148:151], v[32:47]
	v_mfma_f32_32x32x16_f16 v[64:79], v[164:167], v[152:155], v[64:79]
	v_mfma_f32_32x32x16_f16 v[16:31], v[144:147], v[168:171], v[16:31]
	v_mfma_f32_32x32x16_f16 v[48:63], v[168:171], v[148:151], v[48:63]
	v_mfma_f32_32x32x16_f16 v[80:95], v[168:171], v[152:155], v[80:95]
	global_load_dwordx4 v[144:147], v180, s[24:25] offset:0
	global_load_dwordx4 v[148:151], v180, s[26:27] offset:0
	global_load_dwordx4 v[152:155], v180, s[28:29] offset:0
	ds_read_b128 v[164:167], v180 offset:22528
	ds_read_b128 v[168:171], v180 offset:55296
	s_waitcnt vmcnt(12)
	s_waitcnt lgkmcnt(4)
	v_mfma_f32_32x32x16_f16 v[0:15], v[96:99], v[172:175], v[0:15]
	v_mfma_f32_32x32x16_f16 v[32:47], v[172:175], v[100:103], v[32:47]
	v_mfma_f32_32x32x16_f16 v[64:79], v[172:175], v[104:107], v[64:79]
	v_mfma_f32_32x32x16_f16 v[16:31], v[96:99], v[176:179], v[16:31]
	v_mfma_f32_32x32x16_f16 v[48:63], v[176:179], v[100:103], v[48:63]
	v_mfma_f32_32x32x16_f16 v[80:95], v[176:179], v[104:107], v[80:95]
	global_load_dwordx4 v[96:99], v180, s[24:25] offset:1024
	global_load_dwordx4 v[100:103], v180, s[26:27] offset:1024
	global_load_dwordx4 v[104:107], v180, s[28:29] offset:1024
	ds_read_b128 v[172:175], v180 offset:23552
	ds_read_b128 v[176:179], v180 offset:56320
	s_waitcnt vmcnt(12)
	s_waitcnt lgkmcnt(4)
	v_mfma_f32_32x32x16_f16 v[0:15], v[108:111], v[156:159], v[0:15]
	v_mfma_f32_32x32x16_f16 v[32:47], v[156:159], v[112:115], v[32:47]
	v_mfma_f32_32x32x16_f16 v[64:79], v[156:159], v[116:119], v[64:79]
	v_mfma_f32_32x32x16_f16 v[16:31], v[108:111], v[160:163], v[16:31]
	v_mfma_f32_32x32x16_f16 v[48:63], v[160:163], v[112:115], v[48:63]
	v_mfma_f32_32x32x16_f16 v[80:95], v[160:163], v[116:119], v[80:95]
	global_load_dwordx4 v[108:111], v180, s[24:25] offset:2048
	global_load_dwordx4 v[112:115], v180, s[26:27] offset:2048
	global_load_dwordx4 v[116:119], v180, s[28:29] offset:2048
	s_waitcnt vmcnt(12)
	s_waitcnt lgkmcnt(2)
	v_mfma_f32_32x32x16_f16 v[0:15], v[120:123], v[164:167], v[0:15]
	v_mfma_f32_32x32x16_f16 v[32:47], v[164:167], v[124:127], v[32:47]
	v_mfma_f32_32x32x16_f16 v[64:79], v[164:167], v[128:131], v[64:79]
	v_mfma_f32_32x32x16_f16 v[16:31], v[120:123], v[168:171], v[16:31]
	v_mfma_f32_32x32x16_f16 v[48:63], v[168:171], v[124:127], v[48:63]
	v_mfma_f32_32x32x16_f16 v[80:95], v[168:171], v[128:131], v[80:95]
	global_load_dwordx4 v[120:123], v180, s[24:25] offset:3072
	global_load_dwordx4 v[124:127], v180, s[26:27] offset:3072
	global_load_dwordx4 v[128:131], v180, s[28:29] offset:3072
	s_add_u32 s24, s24, 0x1000
	s_addc_u32 s25, s25, 0
	s_add_u32 s26, s26, 0x1000
	s_addc_u32 s27, s27, 0
	s_add_u32 s28, s28, 0x1000
	s_addc_u32 s29, s29, 0
	s_waitcnt vmcnt(12)
	s_waitcnt lgkmcnt(0)
	v_mfma_f32_32x32x16_f16 v[0:15], v[132:135], v[172:175], v[0:15]
	v_mfma_f32_32x32x16_f16 v[32:47], v[172:175], v[136:139], v[32:47]
	v_mfma_f32_32x32x16_f16 v[64:79], v[172:175], v[140:143], v[64:79]
	v_mfma_f32_32x32x16_f16 v[16:31], v[132:135], v[176:179], v[16:31]
	v_mfma_f32_32x32x16_f16 v[48:63], v[176:179], v[136:139], v[48:63]
	v_mfma_f32_32x32x16_f16 v[80:95], v[176:179], v[140:143], v[80:95]
	s_barrier
	ds_read_b128 v[156:159], v180 offset:24576
	ds_read_b128 v[160:163], v180 offset:57344
	ds_read_b128 v[164:167], v180 offset:25600
	ds_read_b128 v[168:171], v180 offset:58368
	global_load_dwordx4 v[132:135], v180, s[24:25] offset:0
	global_load_dwordx4 v[136:139], v180, s[26:27] offset:0
	global_load_dwordx4 v[140:143], v180, s[28:29] offset:0
	ds_read_b128 v[172:175], v180 offset:26624
	ds_read_b128 v[176:179], v180 offset:59392
	s_waitcnt vmcnt(12)
	s_waitcnt lgkmcnt(4)
	v_mfma_f32_32x32x16_f16 v[0:15], v[144:147], v[156:159], v[0:15]
	v_mfma_f32_32x32x16_f16 v[32:47], v[156:159], v[148:151], v[32:47]
	v_mfma_f32_32x32x16_f16 v[64:79], v[156:159], v[152:155], v[64:79]
	v_mfma_f32_32x32x16_f16 v[16:31], v[144:147], v[160:163], v[16:31]
	v_mfma_f32_32x32x16_f16 v[48:63], v[160:163], v[148:151], v[48:63]
	v_mfma_f32_32x32x16_f16 v[80:95], v[160:163], v[152:155], v[80:95]
	global_load_dwordx4 v[144:147], v180, s[24:25] offset:1024
	global_load_dwordx4 v[148:151], v180, s[26:27] offset:1024
	global_load_dwordx4 v[152:155], v180, s[28:29] offset:1024
	ds_read_b128 v[156:159], v180 offset:27648
	ds_read_b128 v[160:163], v180 offset:60416
	s_waitcnt vmcnt(12)
	s_waitcnt lgkmcnt(4)
	v_mfma_f32_32x32x16_f16 v[0:15], v[96:99], v[164:167], v[0:15]
	v_mfma_f32_32x32x16_f16 v[32:47], v[164:167], v[100:103], v[32:47]
	v_mfma_f32_32x32x16_f16 v[64:79], v[164:167], v[104:107], v[64:79]
	v_mfma_f32_32x32x16_f16 v[16:31], v[96:99], v[168:171], v[16:31]
	v_mfma_f32_32x32x16_f16 v[48:63], v[168:171], v[100:103], v[48:63]
	v_mfma_f32_32x32x16_f16 v[80:95], v[168:171], v[104:107], v[80:95]
	global_load_dwordx4 v[96:99], v180, s[24:25] offset:2048
	global_load_dwordx4 v[100:103], v180, s[26:27] offset:2048
	global_load_dwordx4 v[104:107], v180, s[28:29] offset:2048
	ds_read_b128 v[164:167], v180 offset:28672
	ds_read_b128 v[168:171], v180 offset:61440
	s_waitcnt vmcnt(12)
	s_waitcnt lgkmcnt(4)
	v_mfma_f32_32x32x16_f16 v[0:15], v[108:111], v[172:175], v[0:15]
	v_mfma_f32_32x32x16_f16 v[32:47], v[172:175], v[112:115], v[32:47]
	v_mfma_f32_32x32x16_f16 v[64:79], v[172:175], v[116:119], v[64:79]
	v_mfma_f32_32x32x16_f16 v[16:31], v[108:111], v[176:179], v[16:31]
	v_mfma_f32_32x32x16_f16 v[48:63], v[176:179], v[112:115], v[48:63]
	v_mfma_f32_32x32x16_f16 v[80:95], v[176:179], v[116:119], v[80:95]
	global_load_dwordx4 v[108:111], v180, s[24:25] offset:3072
	global_load_dwordx4 v[112:115], v180, s[26:27] offset:3072
	global_load_dwordx4 v[116:119], v180, s[28:29] offset:3072
	s_add_u32 s24, s24, 0x1000
	s_addc_u32 s25, s25, 0
	s_add_u32 s26, s26, 0x1000
	s_addc_u32 s27, s27, 0
	s_add_u32 s28, s28, 0x1000
	s_addc_u32 s29, s29, 0
	ds_read_b128 v[172:175], v180 offset:29696
	ds_read_b128 v[176:179], v180 offset:62464
	s_waitcnt vmcnt(12)
	s_waitcnt lgkmcnt(4)
	v_mfma_f32_32x32x16_f16 v[0:15], v[120:123], v[156:159], v[0:15]
	v_mfma_f32_32x32x16_f16 v[32:47], v[156:159], v[124:127], v[32:47]
	v_mfma_f32_32x32x16_f16 v[64:79], v[156:159], v[128:131], v[64:79]
	v_mfma_f32_32x32x16_f16 v[16:31], v[120:123], v[160:163], v[16:31]
	v_mfma_f32_32x32x16_f16 v[48:63], v[160:163], v[124:127], v[48:63]
	v_mfma_f32_32x32x16_f16 v[80:95], v[160:163], v[128:131], v[80:95]
	ds_read_b128 v[156:159], v180 offset:30720
	ds_read_b128 v[160:163], v180 offset:63488
	s_waitcnt vmcnt(9)
	s_waitcnt lgkmcnt(4)
	v_mfma_f32_32x32x16_f16 v[0:15], v[132:135], v[164:167], v[0:15]
	v_mfma_f32_32x32x16_f16 v[32:47], v[164:167], v[136:139], v[32:47]
	v_mfma_f32_32x32x16_f16 v[64:79], v[164:167], v[140:143], v[64:79]
	v_mfma_f32_32x32x16_f16 v[16:31], v[132:135], v[168:171], v[16:31]
	v_mfma_f32_32x32x16_f16 v[48:63], v[168:171], v[136:139], v[48:63]
	v_mfma_f32_32x32x16_f16 v[80:95], v[168:171], v[140:143], v[80:95]
	ds_read_b128 v[164:167], v180 offset:31744
	ds_read_b128 v[168:171], v180 offset:64512
	s_waitcnt vmcnt(6)
	s_waitcnt lgkmcnt(4)
	v_mfma_f32_32x32x16_f16 v[0:15], v[144:147], v[172:175], v[0:15]
	v_mfma_f32_32x32x16_f16 v[32:47], v[172:175], v[148:151], v[32:47]
	v_mfma_f32_32x32x16_f16 v[64:79], v[172:175], v[152:155], v[64:79]
	v_mfma_f32_32x32x16_f16 v[16:31], v[144:147], v[176:179], v[16:31]
	v_mfma_f32_32x32x16_f16 v[48:63], v[176:179], v[148:151], v[48:63]
	v_mfma_f32_32x32x16_f16 v[80:95], v[176:179], v[152:155], v[80:95]
	s_waitcnt vmcnt(3)
	s_waitcnt lgkmcnt(2)
	v_mfma_f32_32x32x16_f16 v[0:15], v[96:99], v[156:159], v[0:15]
	v_mfma_f32_32x32x16_f16 v[32:47], v[156:159], v[100:103], v[32:47]
	v_mfma_f32_32x32x16_f16 v[64:79], v[156:159], v[104:107], v[64:79]
	v_mfma_f32_32x32x16_f16 v[16:31], v[96:99], v[160:163], v[16:31]
	v_mfma_f32_32x32x16_f16 v[48:63], v[160:163], v[100:103], v[48:63]
	v_mfma_f32_32x32x16_f16 v[80:95], v[160:163], v[104:107], v[80:95]
	s_waitcnt vmcnt(0)
	s_waitcnt lgkmcnt(0)
	v_mfma_f32_32x32x16_f16 v[0:15], v[108:111], v[164:167], v[0:15]
	v_mfma_f32_32x32x16_f16 v[32:47], v[164:167], v[112:115], v[32:47]
	v_mfma_f32_32x32x16_f16 v[64:79], v[164:167], v[116:119], v[64:79]
	v_mfma_f32_32x32x16_f16 v[16:31], v[108:111], v[168:171], v[16:31]
	v_mfma_f32_32x32x16_f16 v[48:63], v[168:171], v[112:115], v[48:63]
	v_mfma_f32_32x32x16_f16 v[80:95], v[168:171], v[116:119], v[80:95]
	s_lshl_b32 s34, s20, 7
	s_lshl_b32 s35, s21, 1
	s_add_u32 s34, s34, s35
	s_cmp_lt_u32 s22, 2
	s_cselect_b32 s36, s6, s8
	s_cselect_b32 s37, s7, s9
	s_cselect_b32 s38, 0x3fb8aa3b, 1.0
	s_lshl_b32 s39, s34, 12
	s_and_b32 s23, s22, 1
	s_lshl_b32 s23, s23, 11
	s_add_u32 s39, s39, s23
	v_add_u32_e32 v186, s39, v180
	s_lshl_b32 s40, s34, 14
	s_lshl_b32 s23, s22, 11
	s_add_u32 s40, s40, s23
	v_add_u32_e32 v187, s40, v180
	s_nop 7
	s_nop 7
	v_mul_f32_e32 v0, 0x4038aa3b, v0
	v_mul_f32_e32 v1, 0x4038aa3b, v1
	v_mul_f32_e32 v2, 0x4038aa3b, v2
	v_mul_f32_e32 v3, 0x4038aa3b, v3
	v_mul_f32_e32 v4, 0x4038aa3b, v4
	v_mul_f32_e32 v5, 0x4038aa3b, v5
	v_mul_f32_e32 v6, 0x4038aa3b, v6
	v_mul_f32_e32 v7, 0x4038aa3b, v7
	v_mul_f32_e32 v8, 0x4038aa3b, v8
	v_mul_f32_e32 v9, 0x4038aa3b, v9
	v_mul_f32_e32 v10, 0x4038aa3b, v10
	v_mul_f32_e32 v11, 0x4038aa3b, v11
	v_mul_f32_e32 v12, 0x4038aa3b, v12
	v_mul_f32_e32 v13, 0x4038aa3b, v13
	v_mul_f32_e32 v14, 0x4038aa3b, v14
	v_mul_f32_e32 v15, 0x4038aa3b, v15
	v_exp_f32_e32 v0, v0
	v_exp_f32_e32 v1, v1
	v_exp_f32_e32 v2, v2
	v_exp_f32_e32 v3, v3
	v_exp_f32_e32 v4, v4
	v_exp_f32_e32 v5, v5
	v_exp_f32_e32 v6, v6
	v_exp_f32_e32 v7, v7
	v_exp_f32_e32 v8, v8
	v_exp_f32_e32 v9, v9
	v_exp_f32_e32 v10, v10
	v_exp_f32_e32 v11, v11
	v_exp_f32_e32 v12, v12
	v_exp_f32_e32 v13, v13
	v_exp_f32_e32 v14, v14
	v_exp_f32_e32 v15, v15
	s_nop 0
	v_add_f32_e32 v0, 1.0, v0
	v_add_f32_e32 v1, 1.0, v1
	v_add_f32_e32 v2, 1.0, v2
	v_add_f32_e32 v3, 1.0, v3
	v_add_f32_e32 v4, 1.0, v4
	v_add_f32_e32 v5, 1.0, v5
	v_add_f32_e32 v6, 1.0, v6
	v_add_f32_e32 v7, 1.0, v7
	v_add_f32_e32 v8, 1.0, v8
	v_add_f32_e32 v9, 1.0, v9
	v_add_f32_e32 v10, 1.0, v10
	v_add_f32_e32 v11, 1.0, v11
	v_add_f32_e32 v12, 1.0, v12
	v_add_f32_e32 v13, 1.0, v13
	v_add_f32_e32 v14, 1.0, v14
	v_add_f32_e32 v15, 1.0, v15
	v_rcp_f32_e32 v0, v0
	v_rcp_f32_e32 v1, v1
	v_rcp_f32_e32 v2, v2
	v_rcp_f32_e32 v3, v3
	v_rcp_f32_e32 v4, v4
	v_rcp_f32_e32 v5, v5
	v_rcp_f32_e32 v6, v6
	v_rcp_f32_e32 v7, v7
	v_rcp_f32_e32 v8, v8
	v_rcp_f32_e32 v9, v9
	v_rcp_f32_e32 v10, v10
	v_rcp_f32_e32 v11, v11
	v_rcp_f32_e32 v12, v12
	v_rcp_f32_e32 v13, v13
	v_rcp_f32_e32 v14, v14
	v_rcp_f32_e32 v15, v15
	s_nop 0
	v_fma_f32 v0, -v0, 2.0, 1.0
	v_fma_f32 v1, -v1, 2.0, 1.0
	v_fma_f32 v2, -v2, 2.0, 1.0
	v_fma_f32 v3, -v3, 2.0, 1.0
	v_fma_f32 v4, -v4, 2.0, 1.0
	v_fma_f32 v5, -v5, 2.0, 1.0
	v_fma_f32 v6, -v6, 2.0, 1.0
	v_fma_f32 v7, -v7, 2.0, 1.0
	v_fma_f32 v8, -v8, 2.0, 1.0
	v_fma_f32 v9, -v9, 2.0, 1.0
	v_fma_f32 v10, -v10, 2.0, 1.0
	v_fma_f32 v11, -v11, 2.0, 1.0
	v_fma_f32 v12, -v12, 2.0, 1.0
	v_fma_f32 v13, -v13, 2.0, 1.0
	v_fma_f32 v14, -v14, 2.0, 1.0
	v_fma_f32 v15, -v15, 2.0, 1.0
	v_mul_f32_e32 v0, s38, v0
	v_mul_f32_e32 v1, s38, v1
	v_mul_f32_e32 v2, s38, v2
	v_mul_f32_e32 v3, s38, v3
	v_mul_f32_e32 v4, s38, v4
	v_mul_f32_e32 v5, s38, v5
	v_mul_f32_e32 v6, s38, v6
	v_mul_f32_e32 v7, s38, v7
	v_mul_f32_e32 v8, s38, v8
	v_mul_f32_e32 v9, s38, v9
	v_mul_f32_e32 v10, s38, v10
	v_mul_f32_e32 v11, s38, v11
	v_mul_f32_e32 v12, s38, v12
	v_mul_f32_e32 v13, s38, v13
	v_mul_f32_e32 v14, s38, v14
	v_mul_f32_e32 v15, s38, v15
	v_cvt_pk_f16_f32 v96, v0, v1
	v_cvt_pk_f16_f32 v97, v2, v3
	v_cvt_pk_f16_f32 v98, v4, v5
	v_cvt_pk_f16_f32 v99, v6, v7
	v_cvt_pk_f16_f32 v100, v8, v9
	v_cvt_pk_f16_f32 v101, v10, v11
	v_cvt_pk_f16_f32 v102, v12, v13
	v_cvt_pk_f16_f32 v103, v14, v15
	global_store_dwordx4 v186, v[96:99], s[36:37]
	global_store_dwordx4 v186, v[100:103], s[36:37] offset:1024
	v_mul_f32_e32 v16, 0x4038aa3b, v16
	v_mul_f32_e32 v17, 0x4038aa3b, v17
	v_mul_f32_e32 v18, 0x4038aa3b, v18
	v_mul_f32_e32 v19, 0x4038aa3b, v19
	v_mul_f32_e32 v20, 0x4038aa3b, v20
	v_mul_f32_e32 v21, 0x4038aa3b, v21
	v_mul_f32_e32 v22, 0x4038aa3b, v22
	v_mul_f32_e32 v23, 0x4038aa3b, v23
	v_mul_f32_e32 v24, 0x4038aa3b, v24
	v_mul_f32_e32 v25, 0x4038aa3b, v25
	v_mul_f32_e32 v26, 0x4038aa3b, v26
	v_mul_f32_e32 v27, 0x4038aa3b, v27
	v_mul_f32_e32 v28, 0x4038aa3b, v28
	v_mul_f32_e32 v29, 0x4038aa3b, v29
	v_mul_f32_e32 v30, 0x4038aa3b, v30
	v_mul_f32_e32 v31, 0x4038aa3b, v31
	v_exp_f32_e32 v16, v16
	v_exp_f32_e32 v17, v17
	v_exp_f32_e32 v18, v18
	v_exp_f32_e32 v19, v19
	v_exp_f32_e32 v20, v20
	v_exp_f32_e32 v21, v21
	v_exp_f32_e32 v22, v22
	v_exp_f32_e32 v23, v23
	v_exp_f32_e32 v24, v24
	v_exp_f32_e32 v25, v25
	v_exp_f32_e32 v26, v26
	v_exp_f32_e32 v27, v27
	v_exp_f32_e32 v28, v28
	v_exp_f32_e32 v29, v29
	v_exp_f32_e32 v30, v30
	v_exp_f32_e32 v31, v31
	s_nop 0
	v_add_f32_e32 v16, 1.0, v16
	v_add_f32_e32 v17, 1.0, v17
	v_add_f32_e32 v18, 1.0, v18
	v_add_f32_e32 v19, 1.0, v19
	v_add_f32_e32 v20, 1.0, v20
	v_add_f32_e32 v21, 1.0, v21
	v_add_f32_e32 v22, 1.0, v22
	v_add_f32_e32 v23, 1.0, v23
	v_add_f32_e32 v24, 1.0, v24
	v_add_f32_e32 v25, 1.0, v25
	v_add_f32_e32 v26, 1.0, v26
	v_add_f32_e32 v27, 1.0, v27
	v_add_f32_e32 v28, 1.0, v28
	v_add_f32_e32 v29, 1.0, v29
	v_add_f32_e32 v30, 1.0, v30
	v_add_f32_e32 v31, 1.0, v31
	v_rcp_f32_e32 v16, v16
	v_rcp_f32_e32 v17, v17
	v_rcp_f32_e32 v18, v18
	v_rcp_f32_e32 v19, v19
	v_rcp_f32_e32 v20, v20
	v_rcp_f32_e32 v21, v21
	v_rcp_f32_e32 v22, v22
	v_rcp_f32_e32 v23, v23
	v_rcp_f32_e32 v24, v24
	v_rcp_f32_e32 v25, v25
	v_rcp_f32_e32 v26, v26
	v_rcp_f32_e32 v27, v27
	v_rcp_f32_e32 v28, v28
	v_rcp_f32_e32 v29, v29
	v_rcp_f32_e32 v30, v30
	v_rcp_f32_e32 v31, v31
	s_nop 0
	v_fma_f32 v16, -v16, 2.0, 1.0
	v_fma_f32 v17, -v17, 2.0, 1.0
	v_fma_f32 v18, -v18, 2.0, 1.0
	v_fma_f32 v19, -v19, 2.0, 1.0
	v_fma_f32 v20, -v20, 2.0, 1.0
	v_fma_f32 v21, -v21, 2.0, 1.0
	v_fma_f32 v22, -v22, 2.0, 1.0
	v_fma_f32 v23, -v23, 2.0, 1.0
	v_fma_f32 v24, -v24, 2.0, 1.0
	v_fma_f32 v25, -v25, 2.0, 1.0
	v_fma_f32 v26, -v26, 2.0, 1.0
	v_fma_f32 v27, -v27, 2.0, 1.0
	v_fma_f32 v28, -v28, 2.0, 1.0
	v_fma_f32 v29, -v29, 2.0, 1.0
	v_fma_f32 v30, -v30, 2.0, 1.0
	v_fma_f32 v31, -v31, 2.0, 1.0
	v_mul_f32_e32 v16, s38, v16
	v_mul_f32_e32 v17, s38, v17
	v_mul_f32_e32 v18, s38, v18
	v_mul_f32_e32 v19, s38, v19
	v_mul_f32_e32 v20, s38, v20
	v_mul_f32_e32 v21, s38, v21
	v_mul_f32_e32 v22, s38, v22
	v_mul_f32_e32 v23, s38, v23
	v_mul_f32_e32 v24, s38, v24
	v_mul_f32_e32 v25, s38, v25
	v_mul_f32_e32 v26, s38, v26
	v_mul_f32_e32 v27, s38, v27
	v_mul_f32_e32 v28, s38, v28
	v_mul_f32_e32 v29, s38, v29
	v_mul_f32_e32 v30, s38, v30
	v_mul_f32_e32 v31, s38, v31
	v_cvt_pk_f16_f32 v104, v16, v17
	v_cvt_pk_f16_f32 v105, v18, v19
	v_cvt_pk_f16_f32 v106, v20, v21
	v_cvt_pk_f16_f32 v107, v22, v23
	v_cvt_pk_f16_f32 v108, v24, v25
	v_cvt_pk_f16_f32 v109, v26, v27
	v_cvt_pk_f16_f32 v110, v28, v29
	v_cvt_pk_f16_f32 v111, v30, v31
	v_add_u32_e32 v186, 0x1000, v186
	global_store_dwordx4 v186, v[104:107], s[36:37]
	global_store_dwordx4 v186, v[108:111], s[36:37] offset:1024
	v_add_u32_e32 v188, 0x2000, v187
	v_add_u32_e32 v189, 0x4000, v187
	v_add_u32_e32 v190, 0x4000, v188
	v_cvt_pk_f16_f32 v112, v32, v33
	v_cvt_pk_f16_f32 v113, v34, v35
	v_cvt_pk_f16_f32 v114, v36, v37
	v_cvt_pk_f16_f32 v115, v38, v39
	global_store_dwordx4 v187, v[112:115], s[10:11] offset:0
	v_cvt_pk_f16_f32 v116, v40, v41
	v_cvt_pk_f16_f32 v117, v42, v43
	v_cvt_pk_f16_f32 v118, v44, v45
	v_cvt_pk_f16_f32 v119, v46, v47
	global_store_dwordx4 v187, v[116:119], s[10:11] offset:1024
	v_cvt_pk_f16_f32 v120, v48, v49
	v_cvt_pk_f16_f32 v121, v50, v51
	v_cvt_pk_f16_f32 v122, v52, v53
	v_cvt_pk_f16_f32 v123, v54, v55
	global_store_dwordx4 v189, v[120:123], s[10:11] offset:0
	v_cvt_pk_f16_f32 v124, v56, v57
	v_cvt_pk_f16_f32 v125, v58, v59
	v_cvt_pk_f16_f32 v126, v60, v61
	v_cvt_pk_f16_f32 v127, v62, v63
	global_store_dwordx4 v189, v[124:127], s[10:11] offset:1024
	v_cvt_pk_f16_f32 v128, v64, v65
	v_cvt_pk_f16_f32 v129, v66, v67
	v_cvt_pk_f16_f32 v130, v68, v69
	v_cvt_pk_f16_f32 v131, v70, v71
	global_store_dwordx4 v188, v[128:131], s[10:11] offset:0
	v_cvt_pk_f16_f32 v132, v72, v73
	v_cvt_pk_f16_f32 v133, v74, v75
	v_cvt_pk_f16_f32 v134, v76, v77
	v_cvt_pk_f16_f32 v135, v78, v79
	global_store_dwordx4 v188, v[132:135], s[10:11] offset:1024
	v_cvt_pk_f16_f32 v136, v80, v81
	v_cvt_pk_f16_f32 v137, v82, v83
	v_cvt_pk_f16_f32 v138, v84, v85
	v_cvt_pk_f16_f32 v139, v86, v87
	global_store_dwordx4 v190, v[136:139], s[10:11] offset:0
	v_cvt_pk_f16_f32 v140, v88, v89
	v_cvt_pk_f16_f32 v141, v90, v91
	v_cvt_pk_f16_f32 v142, v92, v93
	v_cvt_pk_f16_f32 v143, v94, v95
	global_store_dwordx4 v190, v[140:143], s[10:11] offset:1024
	s_endpgm
.Lk1_loader:
	s_sub_u32 s23, s22, 4
	s_lshl_b32 s24, s20, 23
	s_lshl_b32 s25, s21, 8
	s_add_u32 s24, s24, s25
	s_lshl_b32 s25, s23, 17
	s_add_u32 s24, s24, s25
	s_add_u32 s40, s12, s24
	s_addc_u32 s41, s13, 0
	v_lshlrev_b32_e32 v184, 2, v181
	v_lshrrev_b32_e32 v185, 5, v181
	v_lshlrev_b32_e32 v185, 15, v185
	v_and_b32_e32 v186, 31, v181
	v_lshl_add_u32 v185, v186, 4, v185
	s_lshr_b32 s25, s23, 1
	s_lshl_b32 s25, s25, 10
	s_and_b32 s26, s23, 1
	s_lshl_b32 s26, s26, 9
	s_add_u32 s25, s25, s26
	v_add_u32_e32 v185, s25, v185
	global_load_dword v0, v184, s[40:41] nt
	s_add_u32 s42, s40, 0x4000
	s_addc_u32 s43, s41, 0
	global_load_dword v1, v184, s[42:43] nt
	s_add_u32 s42, s40, 0x8000
	s_addc_u32 s43, s41, 0
	global_load_dword v2, v184, s[42:43] nt
	s_add_u32 s42, s40, 0xc000
	s_addc_u32 s43, s41, 0
	global_load_dword v3, v184, s[42:43] nt
	s_add_u32 s42, s40, 0x10000
	s_addc_u32 s43, s41, 0
	global_load_dword v4, v184, s[42:43] nt
	s_add_u32 s42, s40, 0x14000
	s_addc_u32 s43, s41, 0
	global_load_dword v5, v184, s[42:43] nt
	s_add_u32 s42, s40, 0x18000
	s_addc_u32 s43, s41, 0
	global_load_dword v6, v184, s[42:43] nt
	s_add_u32 s42, s40, 0x1c000
	s_addc_u32 s43, s41, 0
	global_load_dword v7, v184, s[42:43] nt
	s_add_u32 s42, s40, 0x80000
	s_addc_u32 s43, s41, 0
	global_load_dword v8, v184, s[42:43] nt
	s_add_u32 s42, s40, 0x84000
	s_addc_u32 s43, s41, 0
	global_load_dword v9, v184, s[42:43] nt
	s_add_u32 s42, s40, 0x88000
	s_addc_u32 s43, s41, 0
	global_load_dword v10, v184, s[42:43] nt
	s_add_u32 s42, s40, 0x8c000
	s_addc_u32 s43, s41, 0
	global_load_dword v11, v184, s[42:43] nt
	s_add_u32 s42, s40, 0x90000
	s_addc_u32 s43, s41, 0
	global_load_dword v12, v184, s[42:43] nt
	s_add_u32 s42, s40, 0x94000
	s_addc_u32 s43, s41, 0
	global_load_dword v13, v184, s[42:43] nt
	s_add_u32 s42, s40, 0x98000
	s_addc_u32 s43, s41, 0
	global_load_dword v14, v184, s[42:43] nt
	s_add_u32 s42, s40, 0x9c000
	s_addc_u32 s43, s41, 0
	global_load_dword v15, v184, s[42:43] nt
	s_add_u32 s42, s40, 0x100000
	s_addc_u32 s43, s41, 0
	global_load_dword v16, v184, s[42:43] nt
	s_add_u32 s42, s40, 0x104000
	s_addc_u32 s43, s41, 0
	global_load_dword v17, v184, s[42:43] nt
	s_add_u32 s42, s40, 0x108000
	s_addc_u32 s43, s41, 0
	global_load_dword v18, v184, s[42:43] nt
	s_add_u32 s42, s40, 0x10c000
	s_addc_u32 s43, s41, 0
	global_load_dword v19, v184, s[42:43] nt
	s_add_u32 s42, s40, 0x110000
	s_addc_u32 s43, s41, 0
	global_load_dword v20, v184, s[42:43] nt
	s_add_u32 s42, s40, 0x114000
	s_addc_u32 s43, s41, 0
	global_load_dword v21, v184, s[42:43] nt
	s_add_u32 s42, s40, 0x118000
	s_addc_u32 s43, s41, 0
	global_load_dword v22, v184, s[42:43] nt
	s_add_u32 s42, s40, 0x11c000
	s_addc_u32 s43, s41, 0
	global_load_dword v23, v184, s[42:43] nt
	s_add_u32 s42, s40, 0x180000
	s_addc_u32 s43, s41, 0
	global_load_dword v24, v184, s[42:43] nt
	s_add_u32 s42, s40, 0x184000
	s_addc_u32 s43, s41, 0
	global_load_dword v25, v184, s[42:43] nt
	s_add_u32 s42, s40, 0x188000
	s_addc_u32 s43, s41, 0
	global_load_dword v26, v184, s[42:43] nt
	s_add_u32 s42, s40, 0x18c000
	s_addc_u32 s43, s41, 0
	global_load_dword v27, v184, s[42:43] nt
	s_add_u32 s42, s40, 0x190000
	s_addc_u32 s43, s41, 0
	global_load_dword v28, v184, s[42:43] nt
	s_add_u32 s42, s40, 0x194000
	s_addc_u32 s43, s41, 0
	global_load_dword v29, v184, s[42:43] nt
	s_add_u32 s42, s40, 0x198000
	s_addc_u32 s43, s41, 0
	global_load_dword v30, v184, s[42:43] nt
	s_add_u32 s42, s40, 0x19c000
	s_addc_u32 s43, s41, 0
	global_load_dword v31, v184, s[42:43] nt
	s_add_u32 s42, s40, 0x200000
	s_addc_u32 s43, s41, 0
	global_load_dword v32, v184, s[42:43] nt
	s_add_u32 s42, s40, 0x204000
	s_addc_u32 s43, s41, 0
	global_load_dword v33, v184, s[42:43] nt
	s_add_u32 s42, s40, 0x208000
	s_addc_u32 s43, s41, 0
	global_load_dword v34, v184, s[42:43] nt
	s_add_u32 s42, s40, 0x20c000
	s_addc_u32 s43, s41, 0
	global_load_dword v35, v184, s[42:43] nt
	s_add_u32 s42, s40, 0x210000
	s_addc_u32 s43, s41, 0
	global_load_dword v36, v184, s[42:43] nt
	s_add_u32 s42, s40, 0x214000
	s_addc_u32 s43, s41, 0
	global_load_dword v37, v184, s[42:43] nt
	s_add_u32 s42, s40, 0x218000
	s_addc_u32 s43, s41, 0
	global_load_dword v38, v184, s[42:43] nt
	s_add_u32 s42, s40, 0x21c000
	s_addc_u32 s43, s41, 0
	global_load_dword v39, v184, s[42:43] nt
	s_add_u32 s42, s40, 0x280000
	s_addc_u32 s43, s41, 0
	global_load_dword v40, v184, s[42:43] nt
	s_add_u32 s42, s40, 0x284000
	s_addc_u32 s43, s41, 0
	global_load_dword v41, v184, s[42:43] nt
	s_add_u32 s42, s40, 0x288000
	s_addc_u32 s43, s41, 0
	global_load_dword v42, v184, s[42:43] nt
	s_add_u32 s42, s40, 0x28c000
	s_addc_u32 s43, s41, 0
	global_load_dword v43, v184, s[42:43] nt
	s_add_u32 s42, s40, 0x290000
	s_addc_u32 s43, s41, 0
	global_load_dword v44, v184, s[42:43] nt
	s_add_u32 s42, s40, 0x294000
	s_addc_u32 s43, s41, 0
	global_load_dword v45, v184, s[42:43] nt
	s_add_u32 s42, s40, 0x298000
	s_addc_u32 s43, s41, 0
	global_load_dword v46, v184, s[42:43] nt
	s_add_u32 s42, s40, 0x29c000
	s_addc_u32 s43, s41, 0
	global_load_dword v47, v184, s[42:43] nt
	s_add_u32 s42, s40, 0x300000
	s_addc_u32 s43, s41, 0
	global_load_dword v48, v184, s[42:43] nt
	s_add_u32 s42, s40, 0x304000
	s_addc_u32 s43, s41, 0
	global_load_dword v49, v184, s[42:43] nt
	s_add_u32 s42, s40, 0x308000
	s_addc_u32 s43, s41, 0
	global_load_dword v50, v184, s[42:43] nt
	s_add_u32 s42, s40, 0x30c000
	s_addc_u32 s43, s41, 0
	global_load_dword v51, v184, s[42:43] nt
	s_add_u32 s42, s40, 0x310000
	s_addc_u32 s43, s41, 0
	global_load_dword v52, v184, s[42:43] nt
	s_add_u32 s42, s40, 0x314000
	s_addc_u32 s43, s41, 0
	global_load_dword v53, v184, s[42:43] nt
	s_add_u32 s42, s40, 0x318000
	s_addc_u32 s43, s41, 0
	global_load_dword v54, v184, s[42:43] nt
	s_add_u32 s42, s40, 0x31c000
	s_addc_u32 s43, s41, 0
	global_load_dword v55, v184, s[42:43] nt
	s_waitcnt vmcnt(48)
	v_cvt_pk_f16_f32 v64, v0, v1
	v_cvt_pk_f16_f32 v65, v2, v3
	v_cvt_pk_f16_f32 v66, v4, v5
	v_cvt_pk_f16_f32 v67, v6, v7
	ds_write_b128 v185, v[64:67] offset:0
	s_add_u32 s42, s40, 0x380000
	s_addc_u32 s43, s41, 0
	global_load_dword v56, v184, s[42:43] nt
	s_add_u32 s42, s40, 0x384000
	s_addc_u32 s43, s41, 0
	global_load_dword v57, v184, s[42:43] nt
	s_add_u32 s42, s40, 0x388000
	s_addc_u32 s43, s41, 0
	global_load_dword v58, v184, s[42:43] nt
	s_add_u32 s42, s40, 0x38c000
	s_addc_u32 s43, s41, 0
	global_load_dword v59, v184, s[42:43] nt
	s_add_u32 s42, s40, 0x390000
	s_addc_u32 s43, s41, 0
	global_load_dword v60, v184, s[42:43] nt
	s_add_u32 s42, s40, 0x394000
	s_addc_u32 s43, s41, 0
	global_load_dword v61, v184, s[42:43] nt
	s_add_u32 s42, s40, 0x398000
	s_addc_u32 s43, s41, 0
	global_load_dword v62, v184, s[42:43] nt
	s_add_u32 s42, s40, 0x39c000
	s_addc_u32 s43, s41, 0
	global_load_dword v63, v184, s[42:43] nt
	s_waitcnt vmcnt(48)
	v_cvt_pk_f16_f32 v68, v8, v9
	v_cvt_pk_f16_f32 v69, v10, v11
	v_cvt_pk_f16_f32 v70, v12, v13
	v_cvt_pk_f16_f32 v71, v14, v15
	ds_write_b128 v185, v[68:71] offset:2048
	s_add_u32 s42, s40, 0x400000
	s_addc_u32 s43, s41, 0
	global_load_dword v0, v184, s[42:43] nt
	s_add_u32 s42, s40, 0x404000
	s_addc_u32 s43, s41, 0
	global_load_dword v1, v184, s[42:43] nt
	s_add_u32 s42, s40, 0x408000
	s_addc_u32 s43, s41, 0
	global_load_dword v2, v184, s[42:43] nt
	s_add_u32 s42, s40, 0x40c000
	s_addc_u32 s43, s41, 0
	global_load_dword v3, v184, s[42:43] nt
	s_add_u32 s42, s40, 0x410000
	s_addc_u32 s43, s41, 0
	global_load_dword v4, v184, s[42:43] nt
	s_add_u32 s42, s40, 0x414000
	s_addc_u32 s43, s41, 0
	global_load_dword v5, v184, s[42:43] nt
	s_add_u32 s42, s40, 0x418000
	s_addc_u32 s43, s41, 0
	global_load_dword v6, v184, s[42:43] nt
	s_add_u32 s42, s40, 0x41c000
	s_addc_u32 s43, s41, 0
	global_load_dword v7, v184, s[42:43] nt
	s_waitcnt vmcnt(48)
	v_cvt_pk_f16_f32 v64, v16, v17
	v_cvt_pk_f16_f32 v65, v18, v19
	v_cvt_pk_f16_f32 v66, v20, v21
	v_cvt_pk_f16_f32 v67, v22, v23
	ds_write_b128 v185, v[64:67] offset:4096
	s_add_u32 s42, s40, 0x480000
	s_addc_u32 s43, s41, 0
	global_load_dword v8, v184, s[42:43] nt
	s_add_u32 s42, s40, 0x484000
	s_addc_u32 s43, s41, 0
	global_load_dword v9, v184, s[42:43] nt
	s_add_u32 s42, s40, 0x488000
	s_addc_u32 s43, s41, 0
	global_load_dword v10, v184, s[42:43] nt
	s_add_u32 s42, s40, 0x48c000
	s_addc_u32 s43, s41, 0
	global_load_dword v11, v184, s[42:43] nt
	s_add_u32 s42, s40, 0x490000
	s_addc_u32 s43, s41, 0
	global_load_dword v12, v184, s[42:43] nt
	s_add_u32 s42, s40, 0x494000
	s_addc_u32 s43, s41, 0
	global_load_dword v13, v184, s[42:43] nt
	s_add_u32 s42, s40, 0x498000
	s_addc_u32 s43, s41, 0
	global_load_dword v14, v184, s[42:43] nt
	s_add_u32 s42, s40, 0x49c000
	s_addc_u32 s43, s41, 0
	global_load_dword v15, v184, s[42:43] nt
	s_waitcnt vmcnt(48)
	v_cvt_pk_f16_f32 v68, v24, v25
	v_cvt_pk_f16_f32 v69, v26, v27
	v_cvt_pk_f16_f32 v70, v28, v29
	v_cvt_pk_f16_f32 v71, v30, v31
	ds_write_b128 v185, v[68:71] offset:6144
	s_add_u32 s42, s40, 0x500000
	s_addc_u32 s43, s41, 0
	global_load_dword v16, v184, s[42:43] nt
	s_add_u32 s42, s40, 0x504000
	s_addc_u32 s43, s41, 0
	global_load_dword v17, v184, s[42:43] nt
	s_add_u32 s42, s40, 0x508000
	s_addc_u32 s43, s41, 0
	global_load_dword v18, v184, s[42:43] nt
	s_add_u32 s42, s40, 0x50c000
	s_addc_u32 s43, s41, 0
	global_load_dword v19, v184, s[42:43] nt
	s_add_u32 s42, s40, 0x510000
	s_addc_u32 s43, s41, 0
	global_load_dword v20, v184, s[42:43] nt
	s_add_u32 s42, s40, 0x514000
	s_addc_u32 s43, s41, 0
	global_load_dword v21, v184, s[42:43] nt
	s_add_u32 s42, s40, 0x518000
	s_addc_u32 s43, s41, 0
	global_load_dword v22, v184, s[42:43] nt
	s_add_u32 s42, s40, 0x51c000
	s_addc_u32 s43, s41, 0
	global_load_dword v23, v184, s[42:43] nt
	s_waitcnt lgkmcnt(0)
	s_barrier
	s_waitcnt vmcnt(48)
	v_cvt_pk_f16_f32 v64, v32, v33
	v_cvt_pk_f16_f32 v65, v34, v35
	v_cvt_pk_f16_f32 v66, v36, v37
	v_cvt_pk_f16_f32 v67, v38, v39
	ds_write_b128 v185, v[64:67] offset:8192
	s_add_u32 s42, s40, 0x580000
	s_addc_u32 s43, s41, 0
	global_load_dword v24, v184, s[42:43] nt
	s_add_u32 s42, s40, 0x584000
	s_addc_u32 s43, s41, 0
	global_load_dword v25, v184, s[42:43] nt
	s_add_u32 s42, s40, 0x588000
	s_addc_u32 s43, s41, 0
	global_load_dword v26, v184, s[42:43] nt
	s_add_u32 s42, s40, 0x58c000
	s_addc_u32 s43, s41, 0
	global_load_dword v27, v184, s[42:43] nt
	s_add_u32 s42, s40, 0x590000
	s_addc_u32 s43, s41, 0
	global_load_dword v28, v184, s[42:43] nt
	s_add_u32 s42, s40, 0x594000
	s_addc_u32 s43, s41, 0
	global_load_dword v29, v184, s[42:43] nt
	s_add_u32 s42, s40, 0x598000
	s_addc_u32 s43, s41, 0
	global_load_dword v30, v184, s[42:43] nt
	s_add_u32 s42, s40, 0x59c000
	s_addc_u32 s43, s41, 0
	global_load_dword v31, v184, s[42:43] nt
	s_waitcnt vmcnt(48)
	v_cvt_pk_f16_f32 v68, v40, v41
	v_cvt_pk_f16_f32 v69, v42, v43
	v_cvt_pk_f16_f32 v70, v44, v45
	v_cvt_pk_f16_f32 v71, v46, v47
	ds_write_b128 v185, v[68:71] offset:10240
	s_add_u32 s42, s40, 0x600000
	s_addc_u32 s43, s41, 0
	global_load_dword v32, v184, s[42:43] nt
	s_add_u32 s42, s40, 0x604000
	s_addc_u32 s43, s41, 0
	global_load_dword v33, v184, s[42:43] nt
	s_add_u32 s42, s40, 0x608000
	s_addc_u32 s43, s41, 0
	global_load_dword v34, v184, s[42:43] nt
	s_add_u32 s42, s40, 0x60c000
	s_addc_u32 s43, s41, 0
	global_load_dword v35, v184, s[42:43] nt
	s_add_u32 s42, s40, 0x610000
	s_addc_u32 s43, s41, 0
	global_load_dword v36, v184, s[42:43] nt
	s_add_u32 s42, s40, 0x614000
	s_addc_u32 s43, s41, 0
	global_load_dword v37, v184, s[42:43] nt
	s_add_u32 s42, s40, 0x618000
	s_addc_u32 s43, s41, 0
	global_load_dword v38, v184, s[42:43] nt
	s_add_u32 s42, s40, 0x61c000
	s_addc_u32 s43, s41, 0
	global_load_dword v39, v184, s[42:43] nt
	s_waitcnt vmcnt(48)
	v_cvt_pk_f16_f32 v64, v48, v49
	v_cvt_pk_f16_f32 v65, v50, v51
	v_cvt_pk_f16_f32 v66, v52, v53
	v_cvt_pk_f16_f32 v67, v54, v55
	ds_write_b128 v185, v[64:67] offset:12288
	s_add_u32 s42, s40, 0x680000
	s_addc_u32 s43, s41, 0
	global_load_dword v40, v184, s[42:43] nt
	s_add_u32 s42, s40, 0x684000
	s_addc_u32 s43, s41, 0
	global_load_dword v41, v184, s[42:43] nt
	s_add_u32 s42, s40, 0x688000
	s_addc_u32 s43, s41, 0
	global_load_dword v42, v184, s[42:43] nt
	s_add_u32 s42, s40, 0x68c000
	s_addc_u32 s43, s41, 0
	global_load_dword v43, v184, s[42:43] nt
	s_add_u32 s42, s40, 0x690000
	s_addc_u32 s43, s41, 0
	global_load_dword v44, v184, s[42:43] nt
	s_add_u32 s42, s40, 0x694000
	s_addc_u32 s43, s41, 0
	global_load_dword v45, v184, s[42:43] nt
	s_add_u32 s42, s40, 0x698000
	s_addc_u32 s43, s41, 0
	global_load_dword v46, v184, s[42:43] nt
	s_add_u32 s42, s40, 0x69c000
	s_addc_u32 s43, s41, 0
	global_load_dword v47, v184, s[42:43] nt
	s_waitcnt vmcnt(48)
	v_cvt_pk_f16_f32 v68, v56, v57
	v_cvt_pk_f16_f32 v69, v58, v59
	v_cvt_pk_f16_f32 v70, v60, v61
	v_cvt_pk_f16_f32 v71, v62, v63
	ds_write_b128 v185, v[68:71] offset:14336
	s_add_u32 s42, s40, 0x700000
	s_addc_u32 s43, s41, 0
	global_load_dword v48, v184, s[42:43] nt
	s_add_u32 s42, s40, 0x704000
	s_addc_u32 s43, s41, 0
	global_load_dword v49, v184, s[42:43] nt
	s_add_u32 s42, s40, 0x708000
	s_addc_u32 s43, s41, 0
	global_load_dword v50, v184, s[42:43] nt
	s_add_u32 s42, s40, 0x70c000
	s_addc_u32 s43, s41, 0
	global_load_dword v51, v184, s[42:43] nt
	s_add_u32 s42, s40, 0x710000
	s_addc_u32 s43, s41, 0
	global_load_dword v52, v184, s[42:43] nt
	s_add_u32 s42, s40, 0x714000
	s_addc_u32 s43, s41, 0
	global_load_dword v53, v184, s[42:43] nt
	s_add_u32 s42, s40, 0x718000
	s_addc_u32 s43, s41, 0
	global_load_dword v54, v184, s[42:43] nt
	s_add_u32 s42, s40, 0x71c000
	s_addc_u32 s43, s41, 0
	global_load_dword v55, v184, s[42:43] nt
	s_waitcnt lgkmcnt(0)
	s_barrier
	s_waitcnt vmcnt(48)
	v_cvt_pk_f16_f32 v64, v0, v1
	v_cvt_pk_f16_f32 v65, v2, v3
	v_cvt_pk_f16_f32 v66, v4, v5
	v_cvt_pk_f16_f32 v67, v6, v7
	ds_write_b128 v185, v[64:67] offset:16384
	s_add_u32 s42, s40, 0x780000
	s_addc_u32 s43, s41, 0
	global_load_dword v56, v184, s[42:43] nt
	s_add_u32 s42, s40, 0x784000
	s_addc_u32 s43, s41, 0
	global_load_dword v57, v184, s[42:43] nt
	s_add_u32 s42, s40, 0x788000
	s_addc_u32 s43, s41, 0
	global_load_dword v58, v184, s[42:43] nt
	s_add_u32 s42, s40, 0x78c000
	s_addc_u32 s43, s41, 0
	global_load_dword v59, v184, s[42:43] nt
	s_add_u32 s42, s40, 0x790000
	s_addc_u32 s43, s41, 0
	global_load_dword v60, v184, s[42:43] nt
	s_add_u32 s42, s40, 0x794000
	s_addc_u32 s43, s41, 0
	global_load_dword v61, v184, s[42:43] nt
	s_add_u32 s42, s40, 0x798000
	s_addc_u32 s43, s41, 0
	global_load_dword v62, v184, s[42:43] nt
	s_add_u32 s42, s40, 0x79c000
	s_addc_u32 s43, s41, 0
	global_load_dword v63, v184, s[42:43] nt
	s_waitcnt vmcnt(48)
	v_cvt_pk_f16_f32 v68, v8, v9
	v_cvt_pk_f16_f32 v69, v10, v11
	v_cvt_pk_f16_f32 v70, v12, v13
	v_cvt_pk_f16_f32 v71, v14, v15
	ds_write_b128 v185, v[68:71] offset:18432
	s_waitcnt vmcnt(40)
	v_cvt_pk_f16_f32 v64, v16, v17
	v_cvt_pk_f16_f32 v65, v18, v19
	v_cvt_pk_f16_f32 v66, v20, v21
	v_cvt_pk_f16_f32 v67, v22, v23
	ds_write_b128 v185, v[64:67] offset:20480
	s_waitcnt vmcnt(32)
	v_cvt_pk_f16_f32 v68, v24, v25
	v_cvt_pk_f16_f32 v69, v26, v27
	v_cvt_pk_f16_f32 v70, v28, v29
	v_cvt_pk_f16_f32 v71, v30, v31
	ds_write_b128 v185, v[68:71] offset:22528
	s_waitcnt lgkmcnt(0)
	s_barrier
	s_waitcnt vmcnt(24)
	v_cvt_pk_f16_f32 v64, v32, v33
	v_cvt_pk_f16_f32 v65, v34, v35
	v_cvt_pk_f16_f32 v66, v36, v37
	v_cvt_pk_f16_f32 v67, v38, v39
	ds_write_b128 v185, v[64:67] offset:24576
	s_waitcnt vmcnt(16)
	v_cvt_pk_f16_f32 v68, v40, v41
	v_cvt_pk_f16_f32 v69, v42, v43
	v_cvt_pk_f16_f32 v70, v44, v45
	v_cvt_pk_f16_f32 v71, v46, v47
	ds_write_b128 v185, v[68:71] offset:26624
	s_waitcnt vmcnt(8)
	v_cvt_pk_f16_f32 v64, v48, v49
	v_cvt_pk_f16_f32 v65, v50, v51
	v_cvt_pk_f16_f32 v66, v52, v53
	v_cvt_pk_f16_f32 v67, v54, v55
	ds_write_b128 v185, v[64:67] offset:28672
	s_waitcnt vmcnt(0)
	v_cvt_pk_f16_f32 v68, v56, v57
	v_cvt_pk_f16_f32 v69, v58, v59
	v_cvt_pk_f16_f32 v70, v60, v61
	v_cvt_pk_f16_f32 v71, v62, v63
	ds_write_b128 v185, v[68:71] offset:30720
	s_waitcnt lgkmcnt(0)
	s_barrier
	s_endpgm

	.amdhsa_kernel _Z7k1_projPKfPKDv8_DF16_S0_S0_S0_PS1_S4_S4_
		.amdhsa_group_segment_fixed_size 65536
		.amdhsa_private_segment_fixed_size 0
		.amdhsa_kernarg_size 64
		.amdhsa_user_sgpr_count 2
		.amdhsa_user_sgpr_dispatch_ptr 0
		.amdhsa_user_sgpr_queue_ptr 0
		.amdhsa_user_sgpr_kernarg_segment_ptr 1
		.amdhsa_user_sgpr_dispatch_id 0
		.amdhsa_user_sgpr_kernarg_preload_length 0
		.amdhsa_user_sgpr_kernarg_preload_offset 0
		.amdhsa_user_sgpr_private_segment_size 0
		.amdhsa_uses_dynamic_stack 0
		.amdhsa_enable_private_segment 0
		.amdhsa_system_sgpr_workgroup_id_x 1
		.amdhsa_system_sgpr_workgroup_id_y 0
		.amdhsa_system_sgpr_workgroup_id_z 0
		.amdhsa_system_sgpr_workgroup_info 0
		.amdhsa_system_vgpr_workitem_id 0
		.amdhsa_next_free_vgpr 192
		.amdhsa_next_free_sgpr 96
		.amdhsa_accum_offset 192
		.amdhsa_reserve_vcc 1
		.amdhsa_float_round_mode_32 0
		.amdhsa_float_round_mode_16_64 0
		.amdhsa_float_denorm_mode_32 3
		.amdhsa_float_denorm_mode_16_64 3
		.amdhsa_dx10_clamp 1
		.amdhsa_ieee_mode 1
		.amdhsa_fp16_overflow 0
		.amdhsa_tg_split 0
		.amdhsa_exception_fp_ieee_invalid_op 0
		.amdhsa_exception_fp_denorm_src 0
		.amdhsa_exception_fp_ieee_div_zero 0
		.amdhsa_exception_fp_ieee_overflow 0
		.amdhsa_exception_fp_ieee_underflow 0
		.amdhsa_exception_fp_ieee_inexact 0
		.amdhsa_exception_int_div_zero 0
	.end_amdhsa_kernel

amdhsa.kernels:
  - .agpr_count:     0
    .args:
      - .actual_access:  read_only
        .address_space:  global
        .offset:         0
        .size:           8
        .value_kind:     global_buffer
      - .actual_access:  read_only
        .address_space:  global
        .offset:         8
        .size:           8
        .value_kind:     global_buffer
      - .actual_access:  read_only
        .address_space:  global
        .offset:         16
        .size:           8
        .value_kind:     global_buffer
      - .actual_access:  read_only
        .address_space:  global
        .offset:         24
        .size:           8
        .value_kind:     global_buffer
      - .actual_access:  write_only
        .address_space:  global
        .offset:         32
        .size:           8
        .value_kind:     global_buffer
      - .actual_access:  write_only
        .address_space:  global
        .offset:         40
        .size:           8
        .value_kind:     global_buffer
    .group_segment_fixed_size: 0
    .kernarg_segment_align: 8
    .kernarg_segment_size: 48
    .language:       OpenCL C
    .language_version:
      - 2
      - 0
    .max_flat_workgroup_size: 256
    .name:           _Z7k0_prepPKfS0_S0_S0_PDv8_DF16_S2_
    .private_segment_fixed_size: 0
    .sgpr_count:     17
    .sgpr_spill_count: 0
    .symbol:         _Z7k0_prepPKfS0_S0_S0_PDv8_DF16_S2_.kd
    .uniform_work_group_size: 1
    .uses_dynamic_stack: false
    .vgpr_count:     14
    .vgpr_spill_count: 0
    .wavefront_size: 64
  - .agpr_count:     0
    .args:
      - .actual_access:  read_only
        .address_space:  global
        .offset:         0
        .size:           8
        .value_kind:     global_buffer
      - .actual_access:  read_only
        .address_space:  global
        .offset:         8
        .size:           8
        .value_kind:     global_buffer
      - .actual_access:  read_only
        .address_space:  global
        .offset:         16
        .size:           8
        .value_kind:     global_buffer
      - .actual_access:  read_only
        .address_space:  global
        .offset:         24
        .size:           8
        .value_kind:     global_buffer
      - .actual_access:  read_only
        .address_space:  global
        .offset:         32
        .size:           8
        .value_kind:     global_buffer
      - .actual_access:  write_only
        .address_space:  global
        .offset:         40
        .size:           8
        .value_kind:     global_buffer
      - .actual_access:  write_only
        .address_space:  global
        .offset:         48
        .size:           8
        .value_kind:     global_buffer
      - .actual_access:  write_only
        .address_space:  global
        .offset:         56
        .size:           8
        .value_kind:     global_buffer
    .group_segment_fixed_size: 65536
    .kernarg_segment_align: 8
    .kernarg_segment_size: 64
    .language:       OpenCL C
    .language_version:
      - 2
      - 0
    .max_flat_workgroup_size: 512
    .name:           _Z7k1_projPKfPKDv8_DF16_S0_S0_S0_PS1_S4_S4_
    .private_segment_fixed_size: 0
    .sgpr_count:     50
    .sgpr_spill_count: 0
    .symbol:         _Z7k1_projPKfPKDv8_DF16_S0_S0_S0_PS1_S4_S4_.kd
    .uniform_work_group_size: 1
    .uses_dynamic_stack: false
    .vgpr_count:     192
    .vgpr_spill_count: 0
    .wavefront_size: 64
  - .agpr_count:     0
    .args:
      - .actual_access:  read_only
        .address_space:  global
        .offset:         0
        .size:           8
        .value_kind:     global_buffer
      - .actual_access:  read_only
        .address_space:  global
        .offset:         8
        .size:           8
        .value_kind:     global_buffer
      - .actual_access:  write_only
        .address_space:  global
        .offset:         16
        .size:           8
        .value_kind:     global_buffer
    .group_segment_fixed_size: 4096
    .kernarg_segment_align: 8
    .kernarg_segment_size: 24
    .language:       OpenCL C
    .language_version:
      - 2
      - 0
    .max_flat_workgroup_size: 512
    .name:           _Z9k2_colsumPKDv8_DF16_S1_Pf
    .private_segment_fixed_size: 0
    .sgpr_count:     30
    .sgpr_spill_count: 0
    .symbol:         _Z9k2_colsumPKDv8_DF16_S1_Pf.kd
    .uniform_work_group_size: 1
    .uses_dynamic_stack: false
    .vgpr_count:     176
    .vgpr_spill_count: 0
    .wavefront_size: 64
  - .agpr_count:     0
    .args:
      - .actual_access:  read_only
        .address_space:  global
        .offset:         0
        .size:           8
        .value_kind:     global_buffer
      - .actual_access:  read_only
        .address_space:  global
        .offset:         8
        .size:           8
        .value_kind:     global_buffer
      - .actual_access:  read_only
        .address_space:  global
        .offset:         16
        .size:           8
        .value_kind:     global_buffer
      - .actual_access:  read_only
        .address_space:  global
        .offset:         24
        .size:           8
        .value_kind:     global_buffer
      - .actual_access:  write_only
        .address_space:  global
        .offset:         32
        .size:           8
        .value_kind:     global_buffer
      - .actual_access:  read_only
        .address_space:  global
        .offset:         40
        .size:           8
        .value_kind:     global_buffer
    .group_segment_fixed_size: 123648
    .kernarg_segment_align: 8
    .kernarg_segment_size: 48
    .language:       OpenCL C
    .language_version:
      - 2
      - 0
    .max_flat_workgroup_size: 512
    .name:           _Z7k3_attnPKDv8_DF16_PKDv4_jS4_S4_PS_PKc
    .private_segment_fixed_size: 0
    .sgpr_count:     46
    .sgpr_spill_count: 0
    .symbol:         _Z7k3_attnPKDv8_DF16_PKDv4_jS4_S4_PS_PKc.kd
    .uniform_work_group_size: 1
    .uses_dynamic_stack: false
    .vgpr_count:     224
    .vgpr_spill_count: 0
    .wavefront_size: 64
  - .agpr_count:     64
    .args:
      - .actual_access:  read_only
        .address_space:  global
        .offset:         0
        .size:           8
        .value_kind:     global_buffer
      - .actual_access:  read_only
        .address_space:  global
        .offset:         8
        .size:           8
        .value_kind:     global_buffer
      - .actual_access:  read_only
        .address_space:  global
        .offset:         16
        .size:           8
        .value_kind:     global_buffer
      - .actual_access:  read_only
        .address_space:  global
        .offset:         24
        .size:           8
        .value_kind:     global_buffer
      - .actual_access:  read_only
        .address_space:  global
        .offset:         32
        .size:           8
        .value_kind:     global_buffer
      - .actual_access:  write_only
        .address_space:  global
        .offset:         40
        .size:           8
        .value_kind:     global_buffer
    .group_segment_fixed_size: 18432
    .kernarg_segment_align: 8
    .kernarg_segment_size: 48
    .language:       OpenCL C
    .language_version:
      - 2
      - 0
    .max_flat_workgroup_size: 256
    .name:           _Z6k4_outPKDv8_DF16_S1_PKfS3_S3_Pf
    .private_segment_fixed_size: 0
    .sgpr_count:     27
    .sgpr_spill_count: 0
    .symbol:         _Z6k4_outPKDv8_DF16_S1_PKfS3_S3_Pf.kd
    .uniform_work_group_size: 1
    .uses_dynamic_stack: false
    .vgpr_count:     216
    .vgpr_spill_count: 0
    .wavefront_size: 64
